# MoBA loops: next-tile LDS-DMA issue moved from the loop top to behind the QK^T MFMAs (s32 + m0 as scalar temps)
# baseline (speedup 1.0000x reference)
; #define LAS __attribute__((address_space(3)))
; __device__ __forceinline__ void moba_unit(const MobaArgs& A, int b, int h, int qb, LAS unsigned char* lds, int wave, bool tables) {
;     ...
;         if (j + 1 < NP) { const int j1 = j + 1; const int kt1 = (j1 < 2) ? q0 + 128 * j1 : 256 * (qb - 1 - ((j1 - 2) >> 1)) + 128 * ((j1 - 2) & 1);
;             LAS unsigned char* sl = lds + L_BUF + (j1 & 1) * 32768;
;             stage_tile<64>(sl, Kh + (size_t)kt1 * 512, Vh + (size_t)kt1 * 512, 512, 512, wid, lane);
;             stage_tile<64>(sl + 16384, Kh + (size_t)(kt1 + 64) * 512, Vh + (size_t)(kt1 + 64) * 512, 512, 512, wid, lane); }
.Ldma_m1_skip:
	s_add_i32 s32, s84, 3
	s_cmp_ge_u32 s32, s95
	s_cbranch_scc1 .Ldma_m1_s_done
	s_cmp_eq_u32 s84, -2
	s_mov_b32 s32, s86
	s_cbranch_scc1 .Ldma_m1_s_k
	s_add_i32 s32, s84, 1
	s_not_b32 s32, s32
	s_lshr_b32 s32, s32, 1
	s_add_i32 s32, s81, s32
	s_lshl_b32 s32, s32, 8
	s_add_i32 m0, s97, 0xffffff80
	s_and_b32 m0, m0, 0x80
	s_or_b32 s32, s32, m0
.Ldma_m1_s_k:
	s_lshl_b32 s32, s32, 10
	v_mov_b32_e32 v216, s32
	v_mov_b32_e32 v217, 0
	s_add_i32 m0, s87, 0x8000
	s_and_b32 m0, m0, 0x8000
	s_add_i32 m0, m0, s82
	v_lshl_add_u64 v[214:215], v[136:137], 0, v[216:217]
	s_nop 0
	global_load_lds_dwordx4 v[214:215], off
	s_add_i32 m0, m0, 0x2000
	v_lshl_add_u64 v[214:215], v[138:139], 0, v[216:217]
	v_add_u32_e32 v216, 0x10000, v216
	global_load_lds_dwordx4 v[214:215], off
	v_lshl_add_u64 v[214:215], v[136:137], 0, v[216:217]
	s_add_i32 m0, m0, 0x2000
	s_nop 0
	global_load_lds_dwordx4 v[214:215], off
	v_lshl_add_u64 v[214:215], v[138:139], 0, v[216:217]
	s_add_i32 m0, m0, 0x2000
	s_nop 0
	global_load_lds_dwordx4 v[214:215], off

; #define LAS __attribute__((address_space(3)))
; __device__ __forceinline__ float fast_exp2(float x) { return __builtin_amdgcn_exp2f(x); }
; __device__ __forceinline__ s16x4 vtr(const LAS unsigned char* p) { return __builtin_bit_cast(s16x4, __builtin_amdgcn_ds_read_tr16_b64_v4i16((LAS v4i16_t*)p)); }
; #define PK8(P, B) __builtin_bit_cast(bf16x8, (u32x4){pk_bf16(P[B], P[B + 1]), pk_bf16(P[B + 2], P[B + 3]), pk_bf16(P[B + 4], P[B + 5]), pk_bf16(P[B + 6], P[B + 7])})
; __device__ __forceinline__ void softmax_pv2(f32x16& a0, f32x16& a1, f32x16& b0, f32x16& b1, f32x16 (&o)[2], float& mref, float& l, f32x16& cn, bool first, LAS float* wsf, ...
;     ...
;     float s0 = 0.f, s1 = 0.f, s2 = 0.f, s3 = 0.f;
; #pragma unroll
;     for (int r = 0; r < 16; ++r) { a0[r] = fast_exp2(a0[r]); a1[r] = fast_exp2(a1[r]); b0[r] = fast_exp2(b0[r]); b1[r] = fast_exp2(b1[r]); s0 += a0[r]; s1 += a1[r]; s2 += b0[r]; s3 += b1[r]; }
;     l += (s0 + s1) + (s2 + s3);
;     bf16x8 pa[8];
;     ...
;     pa[0] = PK8(a0, 0); pa[1] = PK8(a0, 8); pa[2] = PK8(a1, 0); pa[3] = PK8(a1, 8); pa[4] = PK8(b0, 0); pa[5] = PK8(b0, 8); pa[6] = PK8(b1, 0); pa[7] = PK8(b1, 8);
;     ...
;     const int voff = (4 * hi + ((lane & 15) >> 2)) * 64 + ((lane >> 4) & 1) * 32 + (lane & 3) * 8;
; #pragma unroll
;     for (int t = 0; t < 2; ++t) { const LAS unsigned char* vb = (t == 0 ? VsA : VsB) + voff;
;         s16x4 lo[8], hh[8];
; #pragma unroll
;         for (int db = 0; db < 2; ++db)
; #pragma unroll
;             for (int ks = 0; ks < 4; ++ks) { lo[db * 4 + ks] = vtr(vb + db * 4096 + ks * 1024); hh[db * 4 + ks] = vtr(vb + db * 4096 + ks * 1024 + 512); }
;         __builtin_amdgcn_sched_barrier(0);
;     #pragma unroll
;         for (int ks = 0; ks < 4; ++ks)
; #pragma unroll
;             for (int db = 0; db < 2; ++db) { const int i = db * 4 + ks;
;                 const bf16x8 vf = (bf16x8){lo[i][0], lo[i][1], lo[i][2], lo[i][3], hh[i][0], hh[i][1], hh[i][2], hh[i][3]};
;                 o[db] = __builtin_amdgcn_mfma_f32_32x32x16_bf16(pa[4 * t + ks], vf, o[db], 0, 0, 0); }
;         }
.LBB0_646:
	v_exp_f32_e32 v141, v80
	v_exp_f32_e32 v143, v64
	v_exp_f32_e32 v142, v96
	v_exp_f32_e32 v140, v48
	v_exp_f32_e32 v81, v81
	v_exp_f32_e32 v65, v65
	v_exp_f32_e32 v64, v97
	v_exp_f32_e32 v80, v49
	v_exp_f32_e32 v97, v82
	v_exp_f32_e32 v145, v66
	v_exp_f32_e32 v144, v98
	v_exp_f32_e32 v96, v50
	v_exp_f32_e32 v83, v83
	v_exp_f32_e32 v67, v67
	v_exp_f32_e32 v66, v99
	v_exp_f32_e32 v82, v51
	v_exp_f32_e32 v99, v84
	v_exp_f32_e32 v147, v68
	v_exp_f32_e32 v146, v100
	v_exp_f32_e32 v98, v52
	v_pk_add_f32 v[48:49], v[142:143], 0 op_sel_hi:[1,0]
	v_pk_add_f32 v[50:51], v[140:141], 0 op_sel_hi:[1,0]
	v_pk_add_f32 v[48:49], v[64:65], v[48:49]
	v_pk_add_f32 v[50:51], v[80:81], v[50:51]
	v_exp_f32_e32 v85, v85
	v_exp_f32_e32 v69, v69
	v_exp_f32_e32 v68, v101
	v_exp_f32_e32 v84, v53
	v_pk_add_f32 v[48:49], v[144:145], v[48:49]
	v_pk_add_f32 v[50:51], v[96:97], v[50:51]
	v_exp_f32_e32 v101, v86
	v_exp_f32_e32 v149, v70
	v_exp_f32_e32 v148, v102
	v_exp_f32_e32 v100, v54
	v_pk_add_f32 v[48:49], v[66:67], v[48:49]
	v_pk_add_f32 v[50:51], v[82:83], v[50:51]
	v_exp_f32_e32 v87, v87
	v_exp_f32_e32 v71, v71
	v_exp_f32_e32 v70, v103
	v_exp_f32_e32 v86, v55
	v_pk_add_f32 v[48:49], v[146:147], v[48:49]
	v_pk_add_f32 v[50:51], v[98:99], v[50:51]
	v_exp_f32_e32 v151, v88
	v_exp_f32_e32 v103, v72
	v_exp_f32_e32 v102, v104
	v_exp_f32_e32 v150, v56
	v_exp_f32_e32 v153, v89
	v_exp_f32_e32 v73, v73
	v_exp_f32_e32 v72, v105
	v_exp_f32_e32 v152, v57
	v_pk_add_f32 v[48:49], v[68:69], v[48:49]
	v_pk_add_f32 v[50:51], v[84:85], v[50:51]
	v_exp_f32_e32 v169, v90
	v_exp_f32_e32 v89, v74
	v_exp_f32_e32 v88, v106
	v_exp_f32_e32 v168, v58
	v_pk_add_f32 v[48:49], v[148:149], v[48:49]
	v_pk_add_f32 v[50:51], v[100:101], v[50:51]
	v_exp_f32_e32 v171, v91
	v_exp_f32_e32 v75, v75
	v_exp_f32_e32 v74, v107
	v_exp_f32_e32 v170, v59
	v_pk_add_f32 v[48:49], v[70:71], v[48:49]
	v_pk_add_f32 v[50:51], v[86:87], v[50:51]
	v_exp_f32_e32 v173, v92
	v_exp_f32_e32 v91, v76
	v_exp_f32_e32 v90, v108
	v_exp_f32_e32 v172, v60
	v_pk_add_f32 v[48:49], v[102:103], v[48:49]
	v_pk_add_f32 v[50:51], v[150:151], v[50:51]
	v_exp_f32_e32 v175, v93
	v_exp_f32_e32 v77, v77
	v_exp_f32_e32 v76, v109
	v_exp_f32_e32 v174, v61
	v_pk_add_f32 v[48:49], v[72:73], v[48:49]
	v_pk_add_f32 v[50:51], v[152:153], v[50:51]
	v_exp_f32_e32 v177, v94
	v_exp_f32_e32 v93, v78
	v_exp_f32_e32 v92, v110
	v_exp_f32_e32 v176, v62
	v_pk_add_f32 v[48:49], v[88:89], v[48:49]
	v_pk_add_f32 v[50:51], v[168:169], v[50:51]
	v_exp_f32_e32 v179, v95
	v_exp_f32_e32 v79, v79
	v_exp_f32_e32 v78, v111
	v_exp_f32_e32 v178, v63
	v_pk_add_f32 v[48:49], v[74:75], v[48:49]
	v_pk_add_f32 v[50:51], v[170:171], v[50:51]
	v_pk_add_f32 v[48:49], v[90:91], v[48:49]
	v_pk_add_f32 v[50:51], v[172:173], v[50:51]
	v_pk_add_f32 v[48:49], v[76:77], v[48:49]
	v_pk_add_f32 v[50:51], v[174:175], v[50:51]
	v_pk_add_f32 v[48:49], v[92:93], v[48:49]
	v_pk_add_f32 v[50:51], v[176:177], v[50:51]
	v_pk_add_f32 v[48:49], v[78:79], v[48:49]
	v_pk_add_f32 v[50:51], v[178:179], v[50:51]
	v_cvt_pk_bf16_f32 v57, v145, v67
	v_pk_add_f32 v[48:49], v[50:51], v[48:49]
	v_cvt_pk_bf16_f32 v67, v148, v70
	v_cvt_pk_bf16_f32 v70, v90, v76
	v_add3_u32 v76, s94, v161, v163
	v_add_f32_e32 v48, v48, v49
	v_cvt_pk_bf16_f32 v56, v143, v65
	v_cvt_pk_bf16_f32 v65, v144, v66
	v_cvt_pk_bf16_f32 v66, v146, v68
	v_cvt_pk_bf16_f32 v68, v102, v72
	v_cvt_pk_bf16_f32 v72, v140, v80
	v_add3_u32 v140, v76, v165, v157
	v_add_f32_e32 v162, v162, v48
	v_cvt_pk_bf16_f32 v48, v141, v81
	v_cvt_pk_bf16_f32 v49, v97, v83
	v_cvt_pk_bf16_f32 v50, v99, v85
	v_cvt_pk_bf16_f32 v51, v101, v87
	v_cvt_pk_bf16_f32 v58, v147, v69
	v_cvt_pk_bf16_f32 v59, v149, v71
	v_cvt_pk_bf16_f32 v60, v103, v73
	v_cvt_pk_bf16_f32 v61, v89, v75
	v_cvt_pk_bf16_f32 v62, v91, v77
	v_cvt_pk_bf16_f32 v63, v93, v79
	v_cvt_pk_bf16_f32 v69, v88, v74
	v_cvt_pk_bf16_f32 v71, v92, v78
	v_cvt_pk_bf16_f32 v73, v96, v82
	v_cvt_pk_bf16_f32 v74, v98, v84
	v_cvt_pk_bf16_f32 v75, v100, v86
	ds_read_b64_tr_b16 v[76:77], v140 offset:8192
	ds_read_b64_tr_b16 v[78:79], v140 offset:8704
	ds_read_b64_tr_b16 v[80:81], v140 offset:9216
	ds_read_b64_tr_b16 v[82:83], v140 offset:9728
	ds_read_b64_tr_b16 v[84:85], v140 offset:10240
	ds_read_b64_tr_b16 v[86:87], v140 offset:10752
	ds_read_b64_tr_b16 v[88:89], v140 offset:11264
	ds_read_b64_tr_b16 v[90:91], v140 offset:11776
	ds_read_b64_tr_b16 v[92:93], v140 offset:12288
	ds_read_b64_tr_b16 v[94:95], v140 offset:12800
	ds_read_b64_tr_b16 v[96:97], v140 offset:13312
	ds_read_b64_tr_b16 v[98:99], v140 offset:13824
	ds_read_b64_tr_b16 v[100:101], v140 offset:14336
	ds_read_b64_tr_b16 v[102:103], v140 offset:14848
	ds_read_b64_tr_b16 v[104:105], v140 offset:15360
	ds_read_b64_tr_b16 v[106:107], v140 offset:15872
	v_cvt_pk_bf16_f32 v52, v151, v153
	v_cvt_pk_bf16_f32 v53, v169, v171
	v_cvt_pk_bf16_f32 v54, v173, v175
	v_cvt_pk_bf16_f32 v55, v177, v179
	v_cvt_pk_bf16_f32 v64, v142, v64
	v_cvt_pk_bf16_f32 v108, v150, v152
	v_cvt_pk_bf16_f32 v109, v168, v170
	v_cvt_pk_bf16_f32 v110, v172, v174
	v_cvt_pk_bf16_f32 v111, v176, v178
	s_waitcnt lgkmcnt(14)
	v_mfma_f32_32x32x16_bf16 v[16:31], v[48:51], v[76:79], v[16:31]
	s_waitcnt lgkmcnt(6)
	v_mfma_f32_32x32x16_bf16 v[0:15], v[48:51], v[92:95], v[0:15]
	v_mfma_f32_32x32x16_bf16 v[16:31], v[52:55], v[80:83], v[16:31]
	s_waitcnt lgkmcnt(4)
	v_mfma_f32_32x32x16_bf16 v[0:15], v[52:55], v[96:99], v[0:15]
	v_mfma_f32_32x32x16_bf16 v[16:31], v[56:59], v[84:87], v[16:31]
	s_waitcnt lgkmcnt(2)
	v_mfma_f32_32x32x16_bf16 v[0:15], v[56:59], v[100:103], v[0:15]
	ds_read_b64_tr_b16 v[48:49], v140 offset:24576
	ds_read_b64_tr_b16 v[50:51], v140 offset:25088
	ds_read_b64_tr_b16 v[52:53], v140 offset:25600
	ds_read_b64_tr_b16 v[54:55], v140 offset:26112
	ds_read_b64_tr_b16 v[56:57], v140 offset:26624
	ds_read_b64_tr_b16 v[58:59], v140 offset:27136
	ds_read_b64_tr_b16 v[76:77], v140 offset:27648
	ds_read_b64_tr_b16 v[78:79], v140 offset:28160
	v_mfma_f32_32x32x16_bf16 v[16:31], v[60:63], v[88:91], v[16:31]
	ds_read_b64_tr_b16 v[80:81], v140 offset:28672
	ds_read_b64_tr_b16 v[82:83], v140 offset:29184
	ds_read_b64_tr_b16 v[84:85], v140 offset:29696
	ds_read_b64_tr_b16 v[86:87], v140 offset:30208
	ds_read_b64_tr_b16 v[88:89], v140 offset:30720
	ds_read_b64_tr_b16 v[90:91], v140 offset:31232
	ds_read_b64_tr_b16 v[92:93], v140 offset:31744
	ds_read_b64_tr_b16 v[94:95], v140 offset:32256
	s_waitcnt lgkmcnt(14)
	v_mfma_f32_32x32x16_bf16 v[0:15], v[60:63], v[104:107], v[0:15]
	v_mfma_f32_32x32x16_bf16 v[16:31], v[64:67], v[48:51], v[16:31]
	s_waitcnt lgkmcnt(6)
	v_mfma_f32_32x32x16_bf16 v[0:15], v[64:67], v[80:83], v[0:15]
	v_mfma_f32_32x32x16_bf16 v[16:31], v[68:71], v[52:55], v[16:31]
	s_waitcnt lgkmcnt(4)
	v_mfma_f32_32x32x16_bf16 v[0:15], v[68:71], v[84:87], v[0:15]
	v_mfma_f32_32x32x16_bf16 v[16:31], v[72:75], v[56:59], v[16:31]
	s_waitcnt lgkmcnt(2)
	v_mfma_f32_32x32x16_bf16 v[0:15], v[72:75], v[88:91], v[0:15]
	v_mfma_f32_32x32x16_bf16 v[16:31], v[108:111], v[76:79], v[16:31]
	s_waitcnt lgkmcnt(0)
	v_mfma_f32_32x32x16_bf16 v[0:15], v[108:111], v[92:95], v[0:15]

; #define LAS __attribute__((address_space(3)))
; __device__ __forceinline__ void moba_unit(const MobaArgs& A, int b, int h, int qb, LAS unsigned char* lds, int wave, bool tables) {
;     ...
;     for (int j = 0; j < NP; ++j) {
;         asm volatile("s_waitcnt vmcnt(0)" ::: "memory");
;         __syncthreads();
;         if (j + 1 < NP) { const int j1 = j + 1; const int kt1 = (j1 < 2) ? q0 + 128 * j1 : 256 * (qb - 1 - ((j1 - 2) >> 1)) + 128 * ((j1 - 2) & 1);
;             LAS unsigned char* sl = lds + L_BUF + (j1 & 1) * 32768;
;             stage_tile<64>(sl, Kh + (size_t)kt1 * 512, Vh + (size_t)kt1 * 512, 512, 512, wid, lane);
;             stage_tile<64>(sl + 16384, Kh + (size_t)(kt1 + 64) * 512, Vh + (size_t)(kt1 + 64) * 512, 512, 512, wid, lane); }
.LBB0_648:
	s_waitcnt vmcnt(0)
	s_add_i32 s6, s84, 3
	s_cmp_ge_u32 s6, s95
	s_waitcnt vmcnt(0) lgkmcnt(0)
	s_barrier
	s_branch .LBB0_652

; #define LAS __attribute__((address_space(3)))
; __device__ __forceinline__ void moba_unit(const MobaArgs& A, int b, int h, int qb, LAS unsigned char* lds, int wave, bool tables) {
;     ...
;         if (j + 1 < NP) { const int j1 = j + 1; const int kt1 = (j1 < 2) ? q0 + 128 * j1 : 256 * (qb - 1 - ((j1 - 2) >> 1)) + 128 * ((j1 - 2) & 1);
;             LAS unsigned char* sl = lds + L_BUF + (j1 & 1) * 32768;
;             stage_tile<64>(sl, Kh + (size_t)kt1 * 512, Vh + (size_t)kt1 * 512, 512, 512, wid, lane);
;             stage_tile<64>(sl + 16384, Kh + (size_t)(kt1 + 64) * 512, Vh + (size_t)(kt1 + 64) * 512, 512, 512, wid, lane); }
.Ldma_m2_skip:
	s_add_i32 s32, s72, 3
	s_cmp_ge_u32 s32, s76
	s_cbranch_scc1 .Ldma_m2_s_done
	s_cmp_eq_u32 s72, -2
	s_mov_b32 s32, s62
	s_cbranch_scc1 .Ldma_m2_s_k
	s_add_i32 s32, s72, 1
	s_not_b32 s32, s32
	s_lshr_b32 s32, s32, 1
	s_add_i32 s32, s89, s32
	s_lshl_b32 s32, s32, 8
	s_add_i32 m0, s73, 0xffffff80
	s_and_b32 m0, m0, 0x80
	s_or_b32 s32, s32, m0
.Ldma_m2_s_k:
	s_lshl_b32 s32, s32, 10
	v_mov_b32_e32 v216, s32
	v_mov_b32_e32 v217, 0
	s_add_i32 m0, s77, 0x8000
	s_and_b32 m0, m0, 0x8000
	s_add_i32 m0, m0, s81
	v_lshl_add_u64 v[214:215], v[134:135], 0, v[216:217]
	s_nop 0
	global_load_lds_dwordx4 v[214:215], off
	s_add_i32 m0, m0, 0x2000
	v_lshl_add_u64 v[214:215], v[136:137], 0, v[216:217]
	v_add_u32_e32 v216, 0x10000, v216
	global_load_lds_dwordx4 v[214:215], off
	v_lshl_add_u64 v[214:215], v[134:135], 0, v[216:217]
	s_add_i32 m0, m0, 0x2000
	s_nop 0
	global_load_lds_dwordx4 v[214:215], off
	v_lshl_add_u64 v[214:215], v[136:137], 0, v[216:217]
	s_add_i32 m0, m0, 0x2000
	s_nop 0
	global_load_lds_dwordx4 v[214:215], off

; #define LAS __attribute__((address_space(3)))
; __device__ __forceinline__ float fast_exp2(float x) { return __builtin_amdgcn_exp2f(x); }
; __device__ __forceinline__ s16x4 vtr(const LAS unsigned char* p) { return __builtin_bit_cast(s16x4, __builtin_amdgcn_ds_read_tr16_b64_v4i16((LAS v4i16_t*)p)); }
; #define PK8(P, B) __builtin_bit_cast(bf16x8, (u32x4){pk_bf16(P[B], P[B + 1]), pk_bf16(P[B + 2], P[B + 3]), pk_bf16(P[B + 4], P[B + 5]), pk_bf16(P[B + 6], P[B + 7])})
; __device__ __forceinline__ void softmax_pv2(f32x16& a0, f32x16& a1, f32x16& b0, f32x16& b1, f32x16 (&o)[2], float& mref, float& l, f32x16& cn, bool first, LAS float* wsf, ...
;     ...
;     float s0 = 0.f, s1 = 0.f, s2 = 0.f, s3 = 0.f;
; #pragma unroll
;     for (int r = 0; r < 16; ++r) { a0[r] = fast_exp2(a0[r]); a1[r] = fast_exp2(a1[r]); b0[r] = fast_exp2(b0[r]); b1[r] = fast_exp2(b1[r]); s0 += a0[r]; s1 += a1[r]; s2 += b0[r]; s3 += b1[r]; }
;     l += (s0 + s1) + (s2 + s3);
;     bf16x8 pa[8];
;     ...
;     pa[0] = PK8(a0, 0); pa[1] = PK8(a0, 8); pa[2] = PK8(a1, 0); pa[3] = PK8(a1, 8); pa[4] = PK8(b0, 0); pa[5] = PK8(b0, 8); pa[6] = PK8(b1, 0); pa[7] = PK8(b1, 8);
;     ...
;     const int voff = (4 * hi + ((lane & 15) >> 2)) * 64 + ((lane >> 4) & 1) * 32 + (lane & 3) * 8;
; #pragma unroll
;     for (int t = 0; t < 2; ++t) { const LAS unsigned char* vb = (t == 0 ? VsA : VsB) + voff;
;         s16x4 lo[8], hh[8];
; #pragma unroll
;         for (int db = 0; db < 2; ++db)
; #pragma unroll
;             for (int ks = 0; ks < 4; ++ks) { lo[db * 4 + ks] = vtr(vb + db * 4096 + ks * 1024); hh[db * 4 + ks] = vtr(vb + db * 4096 + ks * 1024 + 512); }
;         __builtin_amdgcn_sched_barrier(0);
;     #pragma unroll
;         for (int ks = 0; ks < 4; ++ks)
; #pragma unroll
;             for (int db = 0; db < 2; ++db) { const int i = db * 4 + ks;
;                 const bf16x8 vf = (bf16x8){lo[i][0], lo[i][1], lo[i][2], lo[i][3], hh[i][0], hh[i][1], hh[i][2], hh[i][3]};
;                 o[db] = __builtin_amdgcn_mfma_f32_32x32x16_bf16(pa[4 * t + ks], vf, o[db], 0, 0, 0); }
;         }
.LBB0_724:
	v_exp_f32_e32 v139, v80
	v_exp_f32_e32 v141, v64
	v_exp_f32_e32 v140, v96
	v_exp_f32_e32 v138, v48
	v_exp_f32_e32 v81, v81
	v_exp_f32_e32 v65, v65
	v_exp_f32_e32 v64, v97
	v_exp_f32_e32 v80, v49
	v_exp_f32_e32 v97, v82
	v_exp_f32_e32 v143, v66
	v_exp_f32_e32 v142, v98
	v_exp_f32_e32 v96, v50
	v_exp_f32_e32 v83, v83
	v_exp_f32_e32 v67, v67
	v_exp_f32_e32 v66, v99
	v_exp_f32_e32 v82, v51
	v_exp_f32_e32 v99, v84
	v_exp_f32_e32 v145, v68
	v_exp_f32_e32 v144, v100
	v_exp_f32_e32 v98, v52
	v_pk_add_f32 v[48:49], v[140:141], 0 op_sel_hi:[1,0]
	v_pk_add_f32 v[50:51], v[138:139], 0 op_sel_hi:[1,0]
	v_pk_add_f32 v[48:49], v[64:65], v[48:49]
	v_pk_add_f32 v[50:51], v[80:81], v[50:51]
	v_exp_f32_e32 v85, v85
	v_exp_f32_e32 v69, v69
	v_exp_f32_e32 v68, v101
	v_exp_f32_e32 v84, v53
	v_pk_add_f32 v[48:49], v[142:143], v[48:49]
	v_pk_add_f32 v[50:51], v[96:97], v[50:51]
	v_exp_f32_e32 v101, v86
	v_exp_f32_e32 v147, v70
	v_exp_f32_e32 v146, v102
	v_exp_f32_e32 v100, v54
	v_pk_add_f32 v[48:49], v[66:67], v[48:49]
	v_pk_add_f32 v[50:51], v[82:83], v[50:51]
	v_exp_f32_e32 v87, v87
	v_exp_f32_e32 v71, v71
	v_exp_f32_e32 v70, v103
	v_exp_f32_e32 v86, v55
	v_pk_add_f32 v[48:49], v[144:145], v[48:49]
	v_pk_add_f32 v[50:51], v[98:99], v[50:51]
	v_exp_f32_e32 v149, v88
	v_exp_f32_e32 v103, v72
	v_exp_f32_e32 v102, v104
	v_exp_f32_e32 v148, v56
	v_exp_f32_e32 v151, v89
	v_exp_f32_e32 v73, v73
	v_exp_f32_e32 v72, v105
	v_exp_f32_e32 v150, v57
	v_pk_add_f32 v[48:49], v[68:69], v[48:49]
	v_pk_add_f32 v[50:51], v[84:85], v[50:51]
	v_exp_f32_e32 v169, v90
	v_exp_f32_e32 v89, v74
	v_exp_f32_e32 v88, v106
	v_exp_f32_e32 v168, v58
	v_pk_add_f32 v[48:49], v[146:147], v[48:49]
	v_pk_add_f32 v[50:51], v[100:101], v[50:51]
	v_exp_f32_e32 v171, v91
	v_exp_f32_e32 v75, v75
	v_exp_f32_e32 v74, v107
	v_exp_f32_e32 v170, v59
	v_pk_add_f32 v[48:49], v[70:71], v[48:49]
	v_pk_add_f32 v[50:51], v[86:87], v[50:51]
	v_exp_f32_e32 v173, v92
	v_exp_f32_e32 v91, v76
	v_exp_f32_e32 v90, v108
	v_exp_f32_e32 v172, v60
	v_pk_add_f32 v[48:49], v[102:103], v[48:49]
	v_pk_add_f32 v[50:51], v[148:149], v[50:51]
	v_exp_f32_e32 v175, v93
	v_exp_f32_e32 v77, v77
	v_exp_f32_e32 v76, v109
	v_exp_f32_e32 v174, v61
	v_pk_add_f32 v[48:49], v[72:73], v[48:49]
	v_pk_add_f32 v[50:51], v[150:151], v[50:51]
	v_exp_f32_e32 v177, v94
	v_exp_f32_e32 v93, v78
	v_exp_f32_e32 v92, v110
	v_exp_f32_e32 v176, v62
	v_pk_add_f32 v[48:49], v[88:89], v[48:49]
	v_pk_add_f32 v[50:51], v[168:169], v[50:51]
	v_exp_f32_e32 v179, v95
	v_exp_f32_e32 v79, v79
	v_exp_f32_e32 v78, v111
	v_exp_f32_e32 v178, v63
	v_pk_add_f32 v[48:49], v[74:75], v[48:49]
	v_pk_add_f32 v[50:51], v[170:171], v[50:51]
	v_pk_add_f32 v[48:49], v[90:91], v[48:49]
	v_pk_add_f32 v[50:51], v[172:173], v[50:51]
	v_pk_add_f32 v[48:49], v[76:77], v[48:49]
	v_pk_add_f32 v[50:51], v[174:175], v[50:51]
	v_pk_add_f32 v[48:49], v[92:93], v[48:49]
	v_pk_add_f32 v[50:51], v[176:177], v[50:51]
	v_pk_add_f32 v[48:49], v[78:79], v[48:49]
	v_pk_add_f32 v[50:51], v[178:179], v[50:51]
	v_cvt_pk_bf16_f32 v57, v143, v67
	v_pk_add_f32 v[48:49], v[50:51], v[48:49]
	v_cvt_pk_bf16_f32 v67, v146, v70
	v_cvt_pk_bf16_f32 v70, v90, v76
	v_add3_u32 v76, s74, v162, v163
	v_add_f32_e32 v48, v48, v49
	v_cvt_pk_bf16_f32 v56, v141, v65
	v_cvt_pk_bf16_f32 v65, v142, v66
	v_cvt_pk_bf16_f32 v66, v144, v68
	v_cvt_pk_bf16_f32 v68, v102, v72
	v_cvt_pk_bf16_f32 v72, v138, v80
	v_add3_u32 v138, v76, v165, v157
	v_add_f32_e32 v161, v161, v48
	v_cvt_pk_bf16_f32 v48, v139, v81
	v_cvt_pk_bf16_f32 v49, v97, v83
	v_cvt_pk_bf16_f32 v50, v99, v85
	v_cvt_pk_bf16_f32 v51, v101, v87
	v_cvt_pk_bf16_f32 v58, v145, v69
	v_cvt_pk_bf16_f32 v59, v147, v71
	v_cvt_pk_bf16_f32 v60, v103, v73
	v_cvt_pk_bf16_f32 v61, v89, v75
	v_cvt_pk_bf16_f32 v62, v91, v77
	v_cvt_pk_bf16_f32 v63, v93, v79
	v_cvt_pk_bf16_f32 v69, v88, v74
	v_cvt_pk_bf16_f32 v71, v92, v78
	v_cvt_pk_bf16_f32 v73, v96, v82
	v_cvt_pk_bf16_f32 v74, v98, v84
	v_cvt_pk_bf16_f32 v75, v100, v86
	ds_read_b64_tr_b16 v[76:77], v138 offset:8192
	ds_read_b64_tr_b16 v[78:79], v138 offset:8704
	ds_read_b64_tr_b16 v[80:81], v138 offset:9216
	ds_read_b64_tr_b16 v[82:83], v138 offset:9728
	ds_read_b64_tr_b16 v[84:85], v138 offset:10240
	ds_read_b64_tr_b16 v[86:87], v138 offset:10752
	ds_read_b64_tr_b16 v[88:89], v138 offset:11264
	ds_read_b64_tr_b16 v[90:91], v138 offset:11776
	ds_read_b64_tr_b16 v[92:93], v138 offset:12288
	ds_read_b64_tr_b16 v[94:95], v138 offset:12800
	ds_read_b64_tr_b16 v[96:97], v138 offset:13312
	ds_read_b64_tr_b16 v[98:99], v138 offset:13824
	ds_read_b64_tr_b16 v[100:101], v138 offset:14336
	ds_read_b64_tr_b16 v[102:103], v138 offset:14848
	ds_read_b64_tr_b16 v[104:105], v138 offset:15360
	ds_read_b64_tr_b16 v[106:107], v138 offset:15872
	v_cvt_pk_bf16_f32 v52, v149, v151
	v_cvt_pk_bf16_f32 v53, v169, v171
	v_cvt_pk_bf16_f32 v54, v173, v175
	v_cvt_pk_bf16_f32 v55, v177, v179
	v_cvt_pk_bf16_f32 v64, v140, v64
	v_cvt_pk_bf16_f32 v108, v148, v150
	v_cvt_pk_bf16_f32 v109, v168, v170
	v_cvt_pk_bf16_f32 v110, v172, v174
	v_cvt_pk_bf16_f32 v111, v176, v178
	s_waitcnt lgkmcnt(14)
	v_mfma_f32_32x32x16_bf16 v[16:31], v[48:51], v[76:79], v[16:31]
	s_waitcnt lgkmcnt(6)
	v_mfma_f32_32x32x16_bf16 v[0:15], v[48:51], v[92:95], v[0:15]
	v_mfma_f32_32x32x16_bf16 v[16:31], v[52:55], v[80:83], v[16:31]
	s_waitcnt lgkmcnt(4)
	v_mfma_f32_32x32x16_bf16 v[0:15], v[52:55], v[96:99], v[0:15]
	v_mfma_f32_32x32x16_bf16 v[16:31], v[56:59], v[84:87], v[16:31]
	s_waitcnt lgkmcnt(2)
	v_mfma_f32_32x32x16_bf16 v[0:15], v[56:59], v[100:103], v[0:15]
	ds_read_b64_tr_b16 v[48:49], v138 offset:24576
	ds_read_b64_tr_b16 v[50:51], v138 offset:25088
	ds_read_b64_tr_b16 v[52:53], v138 offset:25600
	ds_read_b64_tr_b16 v[54:55], v138 offset:26112
	ds_read_b64_tr_b16 v[56:57], v138 offset:26624
	ds_read_b64_tr_b16 v[58:59], v138 offset:27136
	ds_read_b64_tr_b16 v[76:77], v138 offset:27648
	ds_read_b64_tr_b16 v[78:79], v138 offset:28160
	v_mfma_f32_32x32x16_bf16 v[16:31], v[60:63], v[88:91], v[16:31]
	ds_read_b64_tr_b16 v[80:81], v138 offset:28672
	ds_read_b64_tr_b16 v[82:83], v138 offset:29184
	ds_read_b64_tr_b16 v[84:85], v138 offset:29696
	ds_read_b64_tr_b16 v[86:87], v138 offset:30208
	ds_read_b64_tr_b16 v[88:89], v138 offset:30720
	ds_read_b64_tr_b16 v[90:91], v138 offset:31232
	ds_read_b64_tr_b16 v[92:93], v138 offset:31744
	ds_read_b64_tr_b16 v[94:95], v138 offset:32256
	s_waitcnt lgkmcnt(14)
	v_mfma_f32_32x32x16_bf16 v[0:15], v[60:63], v[104:107], v[0:15]
	v_mfma_f32_32x32x16_bf16 v[16:31], v[64:67], v[48:51], v[16:31]
	s_waitcnt lgkmcnt(6)
	v_mfma_f32_32x32x16_bf16 v[0:15], v[64:67], v[80:83], v[0:15]
	v_mfma_f32_32x32x16_bf16 v[16:31], v[68:71], v[52:55], v[16:31]
	s_waitcnt lgkmcnt(4)
	v_mfma_f32_32x32x16_bf16 v[0:15], v[68:71], v[84:87], v[0:15]
	v_mfma_f32_32x32x16_bf16 v[16:31], v[72:75], v[56:59], v[16:31]
	s_waitcnt lgkmcnt(2)
	v_mfma_f32_32x32x16_bf16 v[0:15], v[72:75], v[88:91], v[0:15]
	v_mfma_f32_32x32x16_bf16 v[16:31], v[108:111], v[76:79], v[16:31]
	s_waitcnt lgkmcnt(0)
	v_mfma_f32_32x32x16_bf16 v[0:15], v[108:111], v[92:95], v[0:15]

; #define LAS __attribute__((address_space(3)))
; __device__ __forceinline__ void moba_unit(const MobaArgs& A, int b, int h, int qb, LAS unsigned char* lds, int wave, bool tables) {
;     ...
;     for (int j = 0; j < NP; ++j) {
;         asm volatile("s_waitcnt vmcnt(0)" ::: "memory");
;         __syncthreads();
;         if (j + 1 < NP) { const int j1 = j + 1; const int kt1 = (j1 < 2) ? q0 + 128 * j1 : 256 * (qb - 1 - ((j1 - 2) >> 1)) + 128 * ((j1 - 2) & 1);
;             LAS unsigned char* sl = lds + L_BUF + (j1 & 1) * 32768;
;             stage_tile<64>(sl, Kh + (size_t)kt1 * 512, Vh + (size_t)kt1 * 512, 512, 512, wid, lane);
;             stage_tile<64>(sl + 16384, Kh + (size_t)(kt1 + 64) * 512, Vh + (size_t)(kt1 + 64) * 512, 512, 512, wid, lane); }
.LBB0_726:
	s_waitcnt vmcnt(0)
	s_add_i32 s6, s72, 3
	s_cmp_ge_u32 s6, s76
	s_waitcnt vmcnt(0) lgkmcnt(0)
	s_barrier
	s_branch .LBB0_730
